# speedup vs baseline: 1.0201x; 1.0091x over previous
_Z12front_kernel9FrontArgs8PrepArgs8FragArgs:
	s_load_dwordx16 s[4:19], s[0:1], 0x10
	s_cmpk_gt_i32 s2, 0xff
	s_mov_b64 s[20:21], -1
	s_cbranch_scc0 .LBB1_117
	s_load_dword s3, s[0:1], 0x164
	s_add_u32 s34, s0, 0x60
	s_addc_u32 s35, s1, 0
	s_add_i32 s30, s2, 0xffffff00
	s_waitcnt lgkmcnt(0)
	s_add_i32 s20, s3, 0x1ff
	s_ashr_i32 s21, s20, 31
	s_lshr_b32 s21, s21, 23
	s_add_i32 s20, s20, s21
	s_ashr_i32 s22, s20, 9
	s_cmp_ge_i32 s30, s22
	s_mov_b64 s[20:21], -1
	s_cbranch_scc0 .LBB1_103
	s_load_dword s31, s[0:1], 0x2f4
	s_add_u32 s24, s0, 0x1b0
	s_addc_u32 s25, s1, 0
	s_sub_i32 s33, s30, s22
	s_waitcnt lgkmcnt(0)
	s_add_i32 s20, s31, 7
	s_ashr_i32 s21, s20, 31
	s_lshr_b32 s21, s21, 29
	s_add_i32 s20, s20, s21
	s_ashr_i32 s26, s20, 3
	s_cmp_ge_i32 s33, s26
	s_mov_b64 s[20:21], -1
	s_cbranch_scc0 .LBB1_89
	s_cmp_lg_u32 s33, s26
	s_cbranch_scc0 .LBB1_61
	s_not_b32 s26, s26
	s_add_i32 s38, s33, s26
	s_cmpk_lt_u32 s38, 0x100
	s_cselect_b64 s[28:29], -1, 0
	s_cmpk_gt_u32 s38, 0xff
	s_load_dwordx4 s[20:23], s[0:1], 0x50
	s_cselect_b64 s[26:27], -1, 0
	s_and_b64 s[36:37], s[28:29], exec
	s_cselect_b32 s5, s5, s7
	s_cselect_b32 s4, s4, s6
	s_bfe_u32 s36, s38, 0x20006
	s_lshl_b32 s6, s38, 5
	v_lshrrev_b32_e32 v4, 5, v0
	s_and_b32 s37, s6, 0x7e0
	v_and_b32_e32 v5, 31, v0
	s_mul_i32 s6, s36, 0x180
	v_lshrrev_b32_e32 v4, 5, v0
	v_and_b32_e32 v5, 31, v0
	v_add_u32_e32 v6, s6, v4
	v_lshlrev_b32_e32 v6, 11, v6
	v_add3_u32 v6, v6, s37, v5
	v_lshlrev_b32_e32 v6, 2, v6
	v_mul_u32_u24_e32 v7, 33, v4
	v_add_lshl_u32 v7, v7, v5, 2
	s_mov_b64 s[38:39], s[4:5]
	s_and_b64 s[4:5], s[28:29], exec
	v_and_b32_e32 v31, 63, v0
	s_cselect_b32 s7, s9, s13
	s_cselect_b32 s6, s8, s12
	v_lshlrev_b32_e32 v2, 2, v31
	s_cselect_b32 s5, s11, s15
	s_cselect_b32 s4, s10, s14
	global_load_dword v32, v2, s[6:7]
	global_load_dword v33, v2, s[4:5]
	global_load_dword v27, v2, s[6:7] offset:512
	global_load_dword v24, v2, s[6:7] offset:768
	global_load_dword v23, v2, s[6:7] offset:1024
	global_load_dword v1, v2, s[6:7] offset:1280
	global_load_dword v29, v2, s[6:7] offset:256
	global_load_dword v30, v2, s[4:5] offset:256
	global_load_dword v28, v2, s[4:5] offset:512
	global_load_dword v26, v2, s[4:5] offset:768
	global_load_dword v25, v2, s[4:5] offset:1024
	global_load_dword v22, v2, s[4:5] offset:1280
	global_load_dword v36, v6, s[38:39]
	s_add_u32 s38, s38, 0x20000
	s_addc_u32 s39, s39, 0
	global_load_dword v37, v6, s[38:39]
	s_add_u32 s38, s38, 0x20000
	s_addc_u32 s39, s39, 0
	global_load_dword v38, v6, s[38:39]
	s_add_u32 s38, s38, 0x20000
	s_addc_u32 s39, s39, 0
	global_load_dword v39, v6, s[38:39]
	s_add_u32 s38, s38, 0x20000
	s_addc_u32 s39, s39, 0
	global_load_dword v40, v6, s[38:39]
	s_add_u32 s38, s38, 0x20000
	s_addc_u32 s39, s39, 0
	global_load_dword v41, v6, s[38:39]
	s_add_u32 s38, s38, 0x20000
	s_addc_u32 s39, s39, 0
	global_load_dword v42, v6, s[38:39]
	s_add_u32 s38, s38, 0x20000
	s_addc_u32 s39, s39, 0
	global_load_dword v43, v6, s[38:39]
	s_add_u32 s38, s38, 0x20000
	s_addc_u32 s39, s39, 0
	global_load_dword v44, v6, s[38:39]
	s_add_u32 s38, s38, 0x20000
	s_addc_u32 s39, s39, 0
	global_load_dword v45, v6, s[38:39]
	s_add_u32 s38, s38, 0x20000
	s_addc_u32 s39, s39, 0
	global_load_dword v46, v6, s[38:39]
	s_add_u32 s38, s38, 0x20000
	s_addc_u32 s39, s39, 0
	global_load_dword v47, v6, s[38:39]
	s_add_u32 s38, s38, 0x20000
	s_addc_u32 s39, s39, 0
	global_load_dword v48, v6, s[38:39]
	s_add_u32 s38, s38, 0x20000
	s_addc_u32 s39, s39, 0
	global_load_dword v49, v6, s[38:39]
	s_add_u32 s38, s38, 0x20000
	s_addc_u32 s39, s39, 0
	global_load_dword v50, v6, s[38:39]
	s_add_u32 s38, s38, 0x20000
	s_addc_u32 s39, s39, 0
	global_load_dword v51, v6, s[38:39]
	s_add_u32 s38, s38, 0x20000
	s_addc_u32 s39, s39, 0
	global_load_dword v52, v6, s[38:39]
	s_add_u32 s38, s38, 0x20000
	s_addc_u32 s39, s39, 0
	global_load_dword v53, v6, s[38:39]
	s_add_u32 s38, s38, 0x20000
	s_addc_u32 s39, s39, 0
	global_load_dword v54, v6, s[38:39]
	s_add_u32 s38, s38, 0x20000
	s_addc_u32 s39, s39, 0
	global_load_dword v55, v6, s[38:39]
	s_add_u32 s38, s38, 0x20000
	s_addc_u32 s39, s39, 0
	global_load_dword v56, v6, s[38:39]
	s_add_u32 s38, s38, 0x20000
	s_addc_u32 s39, s39, 0
	global_load_dword v57, v6, s[38:39]
	s_add_u32 s38, s38, 0x20000
	s_addc_u32 s39, s39, 0
	global_load_dword v58, v6, s[38:39]
	s_add_u32 s38, s38, 0x20000
	s_addc_u32 s39, s39, 0
	global_load_dword v59, v6, s[38:39]
	s_waitcnt vmcnt(23)
	ds_write_b32 v7, v36
	s_waitcnt vmcnt(22)
	ds_write_b32 v7, v37 offset:2112
	s_waitcnt vmcnt(21)
	ds_write_b32 v7, v38 offset:4224
	s_waitcnt vmcnt(20)
	ds_write_b32 v7, v39 offset:6336
	s_waitcnt vmcnt(19)
	ds_write_b32 v7, v40 offset:8448
	s_waitcnt vmcnt(18)
	ds_write_b32 v7, v41 offset:10560
	s_waitcnt vmcnt(17)
	ds_write_b32 v7, v42 offset:12672
	s_waitcnt vmcnt(16)
	ds_write_b32 v7, v43 offset:14784
	s_waitcnt vmcnt(15)
	ds_write_b32 v7, v44 offset:16896
	s_waitcnt vmcnt(14)
	ds_write_b32 v7, v45 offset:19008
	s_waitcnt vmcnt(13)
	ds_write_b32 v7, v46 offset:21120
	s_waitcnt vmcnt(12)
	ds_write_b32 v7, v47 offset:23232
	s_waitcnt vmcnt(11)
	ds_write_b32 v7, v48 offset:25344
	s_waitcnt vmcnt(10)
	ds_write_b32 v7, v49 offset:27456
	s_waitcnt vmcnt(9)
	ds_write_b32 v7, v50 offset:29568
	s_waitcnt vmcnt(8)
	ds_write_b32 v7, v51 offset:31680
	s_waitcnt vmcnt(7)
	ds_write_b32 v7, v52 offset:33792
	s_waitcnt vmcnt(6)
	ds_write_b32 v7, v53 offset:35904
	s_waitcnt vmcnt(5)
	ds_write_b32 v7, v54 offset:38016
	s_waitcnt vmcnt(4)
	ds_write_b32 v7, v55 offset:40128
	s_waitcnt vmcnt(3)
	ds_write_b32 v7, v56 offset:42240
	s_waitcnt vmcnt(2)
	ds_write_b32 v7, v57 offset:44352
	s_waitcnt vmcnt(1)
	ds_write_b32 v7, v58 offset:46464
	s_waitcnt vmcnt(0)
	ds_write_b32 v7, v59 offset:48576
	s_and_b64 s[40:41], s[28:29], exec
	s_waitcnt lgkmcnt(0)
	s_barrier
	v_lshrrev_b32_e32 v34, 4, v0
	v_and_b32_e32 v35, 28, v34
	v_lshlrev_b32_e32 v37, 2, v35
	s_movk_i32 s4, 0x84
	v_mad_u32_u24 v2, v31, s4, v37
	ds_read2st64_b32 v[12:13], v2 offset1:33
	ds_read2st64_b32 v[8:9], v2 offset0:66 offset1:99
	ds_read2st64_b32 v[6:7], v2 offset0:132 offset1:165
	v_mov_b32_e32 v3, 0
	s_cselect_b32 s5, s19, s21
	s_waitcnt lgkmcnt(2)
	v_add_f32_e32 v2, 0, v12
	v_add_f32_e32 v2, v2, v13
	s_waitcnt lgkmcnt(1)
	v_add_f32_e32 v2, v2, v8
	v_add_f32_e32 v2, v2, v9
	s_waitcnt lgkmcnt(0)
	v_add_f32_e32 v2, v2, v6
	v_add_f32_e32 v2, v2, v7
	v_mov_b32_e32 v10, v9
	v_mov_b32_e32 v11, v8
	v_add_f32_dpp v2, v2, v2 quad_perm:[1,0,3,2] row_mask:0xf bank_mask:0xf bound_ctrl:1
	s_nop 1
	v_add_f32_dpp v2, v2, v2 quad_perm:[2,3,0,1] row_mask:0xf bank_mask:0xf bound_ctrl:1
	s_nop 1
	v_add_f32_dpp v2, v2, v2 row_half_mirror row_mask:0xf bank_mask:0xf bound_ctrl:1
	s_nop 1
	v_add_f32_dpp v2, v2, v2 row_mirror row_mask:0xf bank_mask:0xf bound_ctrl:1
	s_nop 0
	v_readlane_b32 s4, v2, 16
	v_readlane_b32 s8, v2, 48
	v_readlane_b32 s6, v2, 0
	v_readlane_b32 s7, v2, 32
	v_mov_b32_e32 v4, s4
	v_mov_b32_e32 v5, s8
	v_pk_add_f32 v[4:5], s[6:7], v[4:5]
	s_nop 0
	v_add_f32_e32 v2, v4, v5
	v_mul_f32_e32 v2, 0x3b2aaaab, v2
	v_pk_add_f32 v[4:5], v[12:13], v[2:3] op_sel_hi:[1,0] neg_lo:[0,1] neg_hi:[0,1]
	v_pk_add_f32 v[16:17], v[10:11], v[2:3] op_sel_hi:[1,0] neg_lo:[0,1] neg_hi:[0,1]
	v_pk_mul_f32 v[14:15], v[4:5], v[4:5]
	v_mov_b32_e32 v10, v7
	v_mov_b32_e32 v11, v6
	v_pk_mul_f32 v[18:19], v[16:17], v[16:17]
	v_pk_add_f32 v[10:11], v[10:11], v[2:3] op_sel_hi:[1,0] neg_lo:[0,1] neg_hi:[0,1]
	v_add_f32_e32 v2, v14, v15
	v_add_f32_e32 v2, v19, v2
	v_pk_mul_f32 v[20:21], v[10:11], v[10:11]
	v_add_f32_e32 v2, v18, v2
	v_add_f32_e32 v2, v21, v2
	v_add_f32_e32 v2, v20, v2
	s_nop 1
	v_add_f32_dpp v2, v2, v2 quad_perm:[1,0,3,2] row_mask:0xf bank_mask:0xf bound_ctrl:1
	s_nop 1
	v_add_f32_dpp v2, v2, v2 quad_perm:[2,3,0,1] row_mask:0xf bank_mask:0xf bound_ctrl:1
	s_nop 1
	v_add_f32_dpp v2, v2, v2 row_half_mirror row_mask:0xf bank_mask:0xf bound_ctrl:1
	s_nop 1
	v_add_f32_dpp v2, v2, v2 row_mirror row_mask:0xf bank_mask:0xf bound_ctrl:1
	s_nop 0
	v_readlane_b32 s4, v2, 16
	v_readlane_b32 s8, v2, 48
	v_readlane_b32 s6, v2, 0
	v_readlane_b32 s7, v2, 32
	v_mov_b32_e32 v14, s4
	v_mov_b32_e32 v15, s8
	v_pk_add_f32 v[14:15], s[6:7], v[14:15]
	s_mov_b32 s4, 0x800000
	v_add_f32_e32 v2, v14, v15
	v_mov_b32_e32 v14, 0x3727c5ac
	v_fmac_f32_e32 v14, 0x3b2aaaab, v2
	v_mul_f32_e32 v2, 0x4b800000, v14
	v_cmp_gt_f32_e32 vcc, s4, v14
	s_cselect_b32 s4, s18, s20
	s_lshl_b32 s6, s36, 11
	v_cndmask_b32_e32 v2, v14, v2, vcc
	v_rsq_f32_e32 v2, v2
	s_or_b32 s8, s6, s37
	v_mul_f32_e32 v14, 0x45800000, v2
	v_cndmask_b32_e32 v36, v2, v14, vcc
	v_add_u32_e32 v2, s8, v35
	v_mul_u32_u24_e32 v18, 0x180, v2
	v_mul_f32_e32 v2, v4, v36
	s_waitcnt vmcnt(10)
	v_fma_f32 v2, v32, v2, v33
	v_cvt_pk_bf16_f32 v4, v2, s0
	v_or_b32_e32 v2, v18, v31
	v_lshl_add_u64 v[14:15], v[2:3], 1, s[4:5]
	global_store_short v[14:15], v4, off
	s_and_b64 vcc, exec, s[26:27]
	v_mul_f32_e32 v20, v5, v36
	v_lshlrev_b32_e32 v14, 1, v18
	v_lshlrev_b32_e32 v4, 1, v31
	v_add_u32_e32 v18, v18, v31
	s_cbranch_vccz .LBB1_10
	s_waitcnt vmcnt(5)
	v_fma_f32 v5, v29, v20, v30
	v_mov_b32_e32 v15, v3
	v_cvt_pk_bf16_f32 v19, v5, s0
	v_lshl_add_u64 v[38:39], s[20:21], 0, v[14:15]
	v_mov_b32_e32 v5, v3
	v_lshl_add_u64 v[38:39], v[38:39], 0, v[4:5]
	global_store_short v[38:39], v19, off offset:128
	v_mov_b32_e32 v19, v3
	s_mov_b64 s[6:7], 0
	s_branch .LBB1_11

.LBB4_1:
	s_add_i32 s3, s8, s1
	s_add_i32 s6, s3, -4
	s_min_u32 s3, s6, s3
	s_cmp_gt_i32 s3, 1
	s_mul_i32 s6, s3, 0x180
	s_cselect_b32 s7, s2, 0xc400
	s_add_i32 s6, s6, s7
	v_lshl_add_u32 v216, v138, 1, s6
	ds_read_b128 v[172:175], v216
	ds_read_b128 v[176:179], v216 offset:64
	ds_read_b128 v[180:183], v216 offset:12544
	ds_read_b128 v[184:187], v216 offset:12608
	ds_read_b128 v[188:191], v216 offset:128
	ds_read_b128 v[192:195], v216 offset:192
	ds_read_b128 v[196:199], v216 offset:12672
	ds_read_b128 v[200:203], v216 offset:12736
	ds_read_b128 v[204:207], v216 offset:256
	ds_read_b128 v[208:211], v216 offset:320
	ds_read_b128 v[212:215], v216 offset:12800
	ds_read_b128 v[216:219], v216 offset:12864
	s_mul_i32 s6, s3, 0xc00
	s_addk_i32 s6, 0xc00
	s_cmp_lt_i32 s3, 3
	s_cselect_b32 s6, s6, 0
	s_ashr_i32 s7, s6, 31
	s_setprio 1
	s_waitcnt vmcnt(17) lgkmcnt(11)
	v_mfma_f32_16x16x32_bf16 v[94:97], v[172:175], v[50:53], v[94:97]
	s_waitcnt lgkmcnt(9)
	v_mfma_f32_16x16x32_bf16 v[90:93], v[180:183], v[50:53], v[90:93]
	s_waitcnt vmcnt(13)
	v_mfma_f32_16x16x32_bf16 v[86:89], v[172:175], v[58:61], v[86:89]
	v_mfma_f32_16x16x32_bf16 v[82:85], v[180:183], v[58:61], v[82:85]
	s_waitcnt vmcnt(11)
	v_mfma_f32_16x16x32_bf16 v[78:81], v[172:175], v[54:57], v[78:81]
	v_mfma_f32_16x16x32_bf16 v[2:5], v[180:183], v[54:57], v[2:5]
	s_setprio 0
	s_lshl_b64 s[6:7], s[6:7], 1
	v_lshl_add_u64 v[172:173], v[126:127], 0, s[6:7]
	v_lshl_add_u64 v[180:181], v[130:131], 0, s[6:7]
	v_lshl_add_u64 v[174:175], v[128:129], 0, s[6:7]
	global_load_dwordx4 v[50:53], v[172:173], off
	global_load_dwordx4 v[58:61], v[174:175], off
	global_load_dwordx4 v[54:57], v[180:181], off
	s_setprio 1
	v_mfma_f32_16x16x32_bf16 v[94:97], v[176:179], v[30:33], v[94:97]
	s_waitcnt lgkmcnt(8)
	v_mfma_f32_16x16x32_bf16 v[90:93], v[184:187], v[30:33], v[90:93]
	v_mfma_f32_16x16x32_bf16 v[86:89], v[176:179], v[42:45], v[86:89]
	v_mfma_f32_16x16x32_bf16 v[82:85], v[184:187], v[42:45], v[82:85]
	s_waitcnt vmcnt(13)
	v_mfma_f32_16x16x32_bf16 v[78:81], v[176:179], v[34:37], v[78:81]
	v_mfma_f32_16x16x32_bf16 v[2:5], v[184:187], v[34:37], v[2:5]
	s_setprio 0
	global_load_dwordx4 v[30:33], v[172:173], off offset:1024
	global_load_dwordx4 v[42:45], v[174:175], off offset:1024
	global_load_dwordx4 v[34:37], v[180:181], off offset:1024
	s_setprio 1
	s_waitcnt lgkmcnt(7)
	v_mfma_f32_16x16x32_bf16 v[94:97], v[188:191], v[18:21], v[94:97]
	s_waitcnt lgkmcnt(5)
	v_mfma_f32_16x16x32_bf16 v[90:93], v[196:199], v[18:21], v[90:93]
	s_waitcnt vmcnt(15)
	v_mfma_f32_16x16x32_bf16 v[86:89], v[188:191], v[26:29], v[86:89]
	v_mfma_f32_16x16x32_bf16 v[82:85], v[196:199], v[26:29], v[82:85]
	s_waitcnt vmcnt(13)
	v_mfma_f32_16x16x32_bf16 v[78:81], v[188:191], v[22:25], v[78:81]
	v_mfma_f32_16x16x32_bf16 v[2:5], v[196:199], v[22:25], v[2:5]
	s_setprio 0
	global_load_dwordx4 v[18:21], v[172:173], off offset:2048
	global_load_dwordx4 v[26:29], v[174:175], off offset:2048
	global_load_dwordx4 v[22:25], v[180:181], off offset:2048
	s_setprio 1
	v_mfma_f32_16x16x32_bf16 v[94:97], v[192:195], v[6:9], v[94:97]
	s_waitcnt lgkmcnt(4)
	v_mfma_f32_16x16x32_bf16 v[90:93], v[200:203], v[6:9], v[90:93]
	v_mfma_f32_16x16x32_bf16 v[86:89], v[192:195], v[14:17], v[86:89]
	v_mfma_f32_16x16x32_bf16 v[82:85], v[200:203], v[14:17], v[82:85]
	s_waitcnt vmcnt(15)
	v_mfma_f32_16x16x32_bf16 v[78:81], v[192:195], v[10:13], v[78:81]
	v_mfma_f32_16x16x32_bf16 v[2:5], v[200:203], v[10:13], v[2:5]
	s_setprio 0
	global_load_dwordx4 v[6:9], v[172:173], off offset:3072
	global_load_dwordx4 v[14:17], v[174:175], off offset:3072
	global_load_dwordx4 v[10:13], v[180:181], off offset:3072
	s_setprio 1
	s_waitcnt vmcnt(17) lgkmcnt(3)
	v_mfma_f32_16x16x32_bf16 v[94:97], v[204:207], v[62:65], v[94:97]
	s_waitcnt lgkmcnt(1)
	v_mfma_f32_16x16x32_bf16 v[90:93], v[212:215], v[62:65], v[90:93]
	s_waitcnt vmcnt(15)
	v_mfma_f32_16x16x32_bf16 v[86:89], v[204:207], v[66:69], v[86:89]
	v_mfma_f32_16x16x32_bf16 v[82:85], v[212:215], v[66:69], v[82:85]
	s_waitcnt vmcnt(13)
	v_mfma_f32_16x16x32_bf16 v[78:81], v[204:207], v[74:77], v[78:81]
	v_mfma_f32_16x16x32_bf16 v[2:5], v[212:215], v[74:77], v[2:5]
	s_setprio 0
	v_add_co_u32_e32 v172, vcc, s0, v172
	s_nop 1
	v_addc_co_u32_e32 v173, vcc, 0, v173, vcc
	v_add_co_u32_e32 v174, vcc, s0, v174
	s_nop 1
	v_addc_co_u32_e32 v175, vcc, 0, v175, vcc
	v_add_co_u32_e32 v176, vcc, s0, v180
	global_load_dwordx4 v[62:65], v[172:173], off
	global_load_dwordx4 v[66:69], v[174:175], off
	v_addc_co_u32_e32 v177, vcc, 0, v181, vcc
	global_load_dwordx4 v[74:77], v[176:177], off
	s_setprio 1
	v_mfma_f32_16x16x32_bf16 v[94:97], v[208:211], v[46:49], v[94:97]
	s_waitcnt lgkmcnt(0)
	v_mfma_f32_16x16x32_bf16 v[90:93], v[216:219], v[46:49], v[90:93]
	v_mfma_f32_16x16x32_bf16 v[86:89], v[208:211], v[38:41], v[86:89]
	v_mfma_f32_16x16x32_bf16 v[82:85], v[216:219], v[38:41], v[82:85]
	s_waitcnt vmcnt(15)
	v_mfma_f32_16x16x32_bf16 v[78:81], v[208:211], v[70:73], v[78:81]
	v_mfma_f32_16x16x32_bf16 v[2:5], v[216:219], v[70:73], v[2:5]
	s_setprio 0
	global_load_dwordx4 v[46:49], v[172:173], off offset:1024
	global_load_dwordx4 v[38:41], v[174:175], off offset:1024
	global_load_dwordx4 v[70:73], v[176:177], off offset:1024
	s_add_i32 s1, s1, 1
	s_cmp_lg_u32 s1, 3
	s_cbranch_scc1 .LBB4_1
	v_sub_co_u32_e64 v126, s[2:3], s8, 1
	s_and_b64 s[0:1], s[2:3], exec
	v_readfirstlane_b32 s0, v126
	s_cselect_b32 s0, 3, s0
	s_cmp_gt_u32 s0, 1
	s_movk_i32 s1, 0x5f00
	s_mulk_i32 s0, 0x180
	s_cselect_b32 s1, s1, 0xc400
	s_add_i32 s0, s0, s1
	v_lshl_add_u32 v130, v138, 1, s0
	ds_read_b128 v[126:129], v130
	ds_read_b128 v[172:175], v130 offset:64
	ds_read_b128 v[176:179], v130 offset:12544
	ds_read_b128 v[180:183], v130 offset:12608
	ds_read_b128 v[184:187], v130 offset:128
	ds_read_b128 v[188:191], v130 offset:192
	ds_read_b128 v[192:195], v130 offset:12672
	ds_read_b128 v[196:199], v130 offset:12736
	ds_read_b128 v[200:203], v130 offset:256
	ds_read_b128 v[204:207], v130 offset:320
	ds_read_b128 v[208:211], v130 offset:12800
	ds_read_b128 v[212:215], v130 offset:12864
	s_setprio 1
	s_waitcnt vmcnt(17) lgkmcnt(11)
	v_mfma_f32_16x16x32_bf16 v[94:97], v[126:129], v[50:53], v[94:97]
	s_waitcnt lgkmcnt(9)
	v_mfma_f32_16x16x32_bf16 v[50:53], v[176:179], v[50:53], v[90:93]
	s_waitcnt vmcnt(16)
	v_mfma_f32_16x16x32_bf16 v[86:89], v[126:129], v[58:61], v[86:89]
	v_mfma_f32_16x16x32_bf16 v[58:61], v[176:179], v[58:61], v[82:85]
	s_waitcnt vmcnt(15)
	v_mfma_f32_16x16x32_bf16 v[78:81], v[126:129], v[54:57], v[78:81]
	v_mfma_f32_16x16x32_bf16 v[2:5], v[176:179], v[54:57], v[2:5]
	s_setprio 0
	s_setprio 1
	s_waitcnt vmcnt(14)
	v_mfma_f32_16x16x32_bf16 v[54:57], v[172:175], v[30:33], v[94:97]
	s_waitcnt lgkmcnt(8)
	v_mfma_f32_16x16x32_bf16 v[30:33], v[180:183], v[30:33], v[50:53]
	s_waitcnt vmcnt(13)
	v_mfma_f32_16x16x32_bf16 v[50:53], v[172:175], v[42:45], v[86:89]
	v_mfma_f32_16x16x32_bf16 v[42:45], v[180:183], v[42:45], v[58:61]
	s_waitcnt vmcnt(12)
	v_mfma_f32_16x16x32_bf16 v[58:61], v[172:175], v[34:37], v[78:81]
	v_mfma_f32_16x16x32_bf16 v[2:5], v[180:183], v[34:37], v[2:5]
	s_setprio 0
	s_setprio 1
	s_waitcnt vmcnt(11) lgkmcnt(7)
	v_mfma_f32_16x16x32_bf16 v[34:37], v[184:187], v[18:21], v[54:57]
	s_waitcnt lgkmcnt(5)
	v_mfma_f32_16x16x32_bf16 v[18:21], v[192:195], v[18:21], v[30:33]
	s_waitcnt vmcnt(10)
	v_mfma_f32_16x16x32_bf16 v[30:33], v[184:187], v[26:29], v[50:53]
	v_mfma_f32_16x16x32_bf16 v[26:29], v[192:195], v[26:29], v[42:45]
	s_waitcnt vmcnt(9)
	v_mfma_f32_16x16x32_bf16 v[42:45], v[184:187], v[22:25], v[58:61]
	v_mfma_f32_16x16x32_bf16 v[2:5], v[192:195], v[22:25], v[2:5]
	s_setprio 0
	s_setprio 1
	s_waitcnt vmcnt(8)
	v_mfma_f32_16x16x32_bf16 v[22:25], v[188:191], v[6:9], v[34:37]
	s_waitcnt lgkmcnt(4)
	v_mfma_f32_16x16x32_bf16 v[6:9], v[196:199], v[6:9], v[18:21]
	s_waitcnt vmcnt(7)
	v_mfma_f32_16x16x32_bf16 v[18:21], v[188:191], v[14:17], v[30:33]
	v_mfma_f32_16x16x32_bf16 v[14:17], v[196:199], v[14:17], v[26:29]
	s_waitcnt vmcnt(6)
	v_mfma_f32_16x16x32_bf16 v[26:29], v[188:191], v[10:13], v[42:45]
	v_mfma_f32_16x16x32_bf16 v[2:5], v[196:199], v[10:13], v[2:5]
	s_setprio 0
	s_setprio 1
	s_waitcnt vmcnt(5) lgkmcnt(3)
	v_mfma_f32_16x16x32_bf16 v[10:13], v[200:203], v[62:65], v[22:25]
	s_waitcnt lgkmcnt(1)
	v_mfma_f32_16x16x32_bf16 v[6:9], v[208:211], v[62:65], v[6:9]
	s_waitcnt vmcnt(4)
	v_mfma_f32_16x16x32_bf16 v[18:21], v[200:203], v[66:69], v[18:21]
	v_mfma_f32_16x16x32_bf16 v[14:17], v[208:211], v[66:69], v[14:17]
	s_waitcnt vmcnt(3)
	v_mfma_f32_16x16x32_bf16 v[22:25], v[200:203], v[74:77], v[26:29]
	v_mfma_f32_16x16x32_bf16 v[2:5], v[208:211], v[74:77], v[2:5]
	s_setprio 0
	s_setprio 1
	s_waitcnt vmcnt(2)
	v_mfma_f32_16x16x32_bf16 v[10:13], v[204:207], v[46:49], v[10:13]
	s_waitcnt lgkmcnt(0)
	v_mfma_f32_16x16x32_bf16 v[26:29], v[212:215], v[46:49], v[6:9]
	s_waitcnt vmcnt(1)
	v_mfma_f32_16x16x32_bf16 v[94:97], v[204:207], v[38:41], v[18:21]
	v_mfma_f32_16x16x32_bf16 v[128:131], v[212:215], v[38:41], v[14:17]
	s_waitcnt vmcnt(0)
	v_mfma_f32_16x16x32_bf16 v[172:175], v[204:207], v[70:73], v[22:25]
	v_mfma_f32_16x16x32_bf16 v[176:179], v[212:215], v[70:73], v[2:5]
	s_setprio 0
	v_lshlrev_b32_e32 v8, 2, v120
	global_load_dword v82, v8, s[16:17]
	v_lshlrev_b32_e32 v220, 2, v122
	v_lshlrev_b32_e32 v221, 2, v118
	global_load_dword v220, v220, s[16:17]
	global_load_dword v221, v221, s[16:17]
	s_mul_i32 s0, s8, 0xc00
	v_add_u32_e32 v2, v171, v145
	v_mov_b32_e32 v9, 0
	s_add_u32 s0, s24, s0
	v_add_f32_e32 v83, v165, v10
	v_add_u32_e32 v7, 0x300, v2
	v_add_u32_e32 v93, 0x900, v2
	v_add_u32_e32 v126, 0xf00, v2
	v_lshl_add_u64 v[2:3], s[22:23], 0, v[8:9]
	s_addc_u32 s1, s25, 0
	v_lshlrev_b32_e32 v6, 1, v124
	v_add_f32_e32 v86, v164, v11
	v_add_f32_e32 v87, v163, v12
	v_add_f32_e32 v88, v162, v13
	v_add_f32_e32 v89, v170, v26
	v_add_f32_e32 v124, v169, v27
	v_add_f32_e32 v127, v168, v28
	v_add_f32_e32 v145, v167, v29
	v_lshlrev_b64 v[78:79], 2, v[122:123]
	v_lshlrev_b32_e32 v9, 4, v7
	v_lshlrev_b32_e32 v18, 4, v93
	v_lshlrev_b32_e32 v4, 4, v126
	v_lshl_add_u64 v[84:85], v[2:3], 0, v[116:117]
	v_lshl_add_u64 v[14:15], v[100:101], 1, s[0:1]
	v_lshl_add_u64 v[16:17], v[98:99], 1, s[0:1]
	v_lshl_add_u64 v[80:81], s[16:17], 0, v[78:79]
	v_lshl_add_u64 v[90:91], v[2:3], 0, v[114:115]
	v_lshl_add_u64 v[162:163], v[2:3], 0, v[112:113]
	v_lshl_add_u64 v[164:165], v[2:3], 0, v[110:111]
	v_lshl_add_u64 v[168:169], v[2:3], 0, v[108:109]
	v_lshl_add_u64 v[170:171], v[2:3], 0, v[106:107]
	v_lshl_add_u64 v[180:181], v[2:3], 0, v[104:105]
	v_lshl_add_u64 v[182:183], v[2:3], 0, v[102:103]
	global_load_dwordx4 v[62:65], v9, s[0:1]
	global_load_dwordx4 v[38:41], v9, s[0:1] offset:1024
	global_load_dwordx4 v[58:61], v18, s[0:1]
	global_load_dwordx4 v[34:37], v18, s[0:1] offset:1024
	global_load_dwordx4 v[54:57], v4, s[0:1]
	global_load_dwordx4 v[10:13], v4, s[0:1] offset:1024
	global_load_dwordx4 v[50:53], v6, s[0:1] offset:1024
	global_load_dwordx4 v[26:29], v6, s[0:1] offset:2048
	global_load_dwordx4 v[74:77], v6, s[0:1]
	s_nop 0
	global_load_dwordx4 v[2:5], v4, s[0:1] offset:2048
	s_nop 0
	global_load_dwordx4 v[66:69], v[14:15], off
	global_load_dwordx4 v[30:33], v9, s[0:1] offset:2048
	global_load_dwordx4 v[46:49], v[14:15], off offset:1024
	global_load_dwordx4 v[22:25], v[14:15], off offset:2048
	global_load_dwordx4 v[70:73], v[16:17], off
	s_nop 0
	global_load_dwordx4 v[18:21], v18, s[0:1] offset:2048
	s_nop 0
	global_load_dwordx4 v[42:45], v[16:17], off offset:1024
	s_nop 0
	global_load_dwordx4 v[14:17], v[16:17], off offset:2048
	v_add_f32_e32 v167, v158, v131
	v_add_f32_e32 v151, v151, v178
	v_cmp_ne_u32_e32 vcc, 0, v136
	v_cmp_eq_u32_e64 s[0:1], 0, v136
	s_waitcnt vmcnt(18)
	v_add_f32_e32 v123, v82, v83
	v_add_f32_e32 v122, v82, v86
	v_add_f32_e32 v120, v82, v87
	v_add_f32_e32 v92, v82, v88
	v_add_f32_e32 v89, v82, v89
	v_add_f32_e32 v86, v82, v124
	v_add_f32_e32 v83, v82, v127
	v_add_f32_e32 v9, v82, v145
	global_store_dword v[84:85], v123, off
	global_store_dword v[90:91], v122, off
	global_store_dword v[162:163], v120, off
	global_store_dword v[164:165], v92, off
	global_store_dword v[168:169], v89, off
	global_store_dword v[170:171], v86, off
	global_store_dword v[180:181], v83, off
	global_store_dword v[182:183], v9, off
	v_add_f32_e32 v87, v157, v94
	v_lshl_add_u64 v[84:85], s[22:23], 0, v[78:79]
	v_add_f32_e32 v88, v156, v95
	v_add_f32_e32 v90, v155, v96
	v_add_f32_e32 v91, v154, v97
	v_add_f32_e32 v95, v161, v128
	v_add_f32_e32 v127, v160, v129
	v_add_f32_e32 v145, v159, v130
	v_lshlrev_b64 v[80:81], 2, v[118:119]
	v_lshl_add_u64 v[128:129], v[84:85], 0, v[116:117]
	v_lshl_add_u64 v[96:97], s[16:17], 0, v[80:81]
	v_lshl_add_u64 v[130:131], v[84:85], 0, v[114:115]
	v_lshl_add_u64 v[154:155], v[84:85], 0, v[112:113]
	v_lshl_add_u64 v[156:157], v[84:85], 0, v[110:111]
	v_lshl_add_u64 v[158:159], v[84:85], 0, v[108:109]
	v_lshl_add_u64 v[160:161], v[84:85], 0, v[106:107]
	v_lshl_add_u64 v[162:163], v[84:85], 0, v[104:105]
	v_lshl_add_u64 v[164:165], v[84:85], 0, v[102:103]
	v_add_f32_e32 v124, v220, v87
	v_add_f32_e32 v119, v220, v88
	v_add_f32_e32 v118, v220, v90
	v_add_f32_e32 v94, v220, v91
	v_add_f32_e32 v90, v220, v95
	v_add_f32_e32 v87, v220, v127
	v_add_f32_e32 v84, v220, v145
	v_add_f32_e32 v82, v220, v167
	global_store_dword v[128:129], v124, off
	global_store_dword v[130:131], v119, off
	global_store_dword v[154:155], v118, off
	global_store_dword v[156:157], v94, off
	global_store_dword v[158:159], v90, off
	global_store_dword v[160:161], v87, off
	global_store_dword v[162:163], v84, off
	global_store_dword v[164:165], v82, off
	v_lshl_add_u64 v[96:97], s[22:23], 0, v[80:81]
	v_add_f32_e32 v88, v150, v172
	v_add_f32_e32 v91, v148, v173
	v_add_f32_e32 v95, v147, v174
	v_add_f32_e32 v129, v146, v175
	v_add_f32_e32 v150, v152, v177
	v_add_f32_e32 v152, v149, v179
	v_lshl_add_u64 v[116:117], v[96:97], 0, v[116:117]
	v_lshl_add_u64 v[130:131], v[96:97], 0, v[114:115]
	v_lshl_add_u64 v[146:147], v[96:97], 0, v[112:113]
	v_lshl_add_u64 v[110:111], v[96:97], 0, v[110:111]
	v_lshl_add_u64 v[148:149], v[96:97], 0, v[108:109]
	v_lshl_add_u64 v[106:107], v[96:97], 0, v[106:107]
	v_lshl_add_u64 v[104:105], v[96:97], 0, v[104:105]
	v_lshl_add_u64 v[96:97], v[96:97], 0, v[102:103]
	v_add_f32_e32 v102, 0, v123
	v_fma_f32 v103, v123, v123, 0
	v_add_f32_e32 v108, v102, v124
	v_fmac_f32_e32 v103, v124, v124
	v_add_f32_e32 v145, v153, v176
	v_mov_b32_e32 v128, 0x12600
	v_lshlrev_b32_e32 v127, 5, v135
	v_lshl_or_b32 v128, v121, 2, v128
	v_add_f32_e32 v114, v221, v88
	v_add_f32_e32 v108, v108, v114
	v_fmac_f32_e32 v103, v114, v114
	v_add_f32_e32 v112, v221, v91
	v_add_f32_e32 v109, v221, v95
	v_add_f32_e32 v102, v221, v129
	v_add_f32_e32 v95, v221, v145
	v_add_f32_e32 v91, v221, v150
	v_add_f32_e32 v88, v221, v151
	v_add_f32_e32 v85, v221, v152
	global_store_dword v[116:117], v114, off
	global_store_dword v[130:131], v112, off
	global_store_dword v[146:147], v109, off
	global_store_dword v[110:111], v102, off
	global_store_dword v[148:149], v95, off
	global_store_dword v[106:107], v91, off
	global_store_dword v[104:105], v88, off
	global_store_dword v[96:97], v85, off
	v_add_f32_dpp v96, v108, v108 quad_perm:[1,0,3,2] row_mask:0xf bank_mask:0xf bound_ctrl:1
	v_add_f32_dpp v97, v103, v103 quad_perm:[1,0,3,2] row_mask:0xf bank_mask:0xf bound_ctrl:1
	s_nop 0
	v_add_f32_dpp v96, v96, v96 quad_perm:[2,3,0,1] row_mask:0xf bank_mask:0xf bound_ctrl:1
	v_add_f32_dpp v103, v97, v97 quad_perm:[2,3,0,1] row_mask:0xf bank_mask:0xf bound_ctrl:1
	s_nop 0
	v_add_f32_dpp v97, v96, v96 row_half_mirror row_mask:0xf bank_mask:0xf bound_ctrl:1
	v_add_f32_dpp v104, v103, v103 row_half_mirror row_mask:0xf bank_mask:0xf bound_ctrl:1
	v_lshlrev_b32_e32 v96, 2, v121
	v_mov_b32_dpp v103, v97 row_mirror row_mask:0xf bank_mask:0xf bound_ctrl:1
	v_mov_b32_dpp v105, v104 row_mirror row_mask:0xf bank_mask:0xf bound_ctrl:1
	s_and_saveexec_b64 s[6:7], s[0:1]
	s_cbranch_execz .LBB4_4
	v_add_f32_e32 v97, v97, v103
	v_add_u32_e32 v103, v128, v127
	s_mov_b32 s9, 0x12a00
	v_add_f32_e32 v104, v104, v105
	ds_write_b32 v103, v97
	v_or3_b32 v97, v127, v96, s9
	ds_write_b32 v97, v104

	.amdhsa_kernel _Z12chain_kernelILi0EEv9ChainArgs
		.amdhsa_group_segment_fixed_size 77312
		.amdhsa_private_segment_fixed_size 0
		.amdhsa_kernarg_size 144
		.amdhsa_user_sgpr_count 2
		.amdhsa_user_sgpr_dispatch_ptr 0
		.amdhsa_user_sgpr_queue_ptr 0
		.amdhsa_user_sgpr_kernarg_segment_ptr 1
		.amdhsa_user_sgpr_dispatch_id 0
		.amdhsa_user_sgpr_kernarg_preload_length 0
		.amdhsa_user_sgpr_kernarg_preload_offset 0
		.amdhsa_user_sgpr_private_segment_size 0
		.amdhsa_uses_dynamic_stack 0
		.amdhsa_enable_private_segment 0
		.amdhsa_system_sgpr_workgroup_id_x 1
		.amdhsa_system_sgpr_workgroup_id_y 0
		.amdhsa_system_sgpr_workgroup_id_z 0
		.amdhsa_system_sgpr_workgroup_info 0
		.amdhsa_system_vgpr_workitem_id 0
		.amdhsa_next_free_vgpr 224
		.amdhsa_next_free_sgpr 96
		.amdhsa_accum_offset 224
		.amdhsa_reserve_vcc 1
		.amdhsa_float_round_mode_32 0
		.amdhsa_float_round_mode_16_64 0
		.amdhsa_float_denorm_mode_32 3
		.amdhsa_float_denorm_mode_16_64 3
		.amdhsa_dx10_clamp 1
		.amdhsa_ieee_mode 1
		.amdhsa_fp16_overflow 0
		.amdhsa_tg_split 0
		.amdhsa_exception_fp_ieee_invalid_op 0
		.amdhsa_exception_fp_denorm_src 0
		.amdhsa_exception_fp_ieee_div_zero 0
		.amdhsa_exception_fp_ieee_overflow 0
		.amdhsa_exception_fp_ieee_underflow 0
		.amdhsa_exception_fp_ieee_inexact 0
		.amdhsa_exception_int_div_zero 0
	.end_amdhsa_kernel

amdhsa.kernels:
  - .agpr_count:     0
    .args:
      - .offset:         0
        .size:           4
        .value_kind:     by_value
      - .actual_access:  read_only
        .address_space:  global
        .offset:         8
        .size:           8
        .value_kind:     global_buffer
      - .actual_access:  read_only
        .address_space:  global
        .offset:         16
        .size:           8
        .value_kind:     global_buffer
      - .actual_access:  read_only
        .address_space:  global
        .offset:         24
        .size:           8
        .value_kind:     global_buffer
      - .actual_access:  read_only
        .address_space:  global
        .offset:         32
        .size:           8
        .value_kind:     global_buffer
      - .offset:         40
        .size:           4
        .value_kind:     by_value
      - .actual_access:  read_only
        .address_space:  global
        .offset:         48
        .size:           8
        .value_kind:     global_buffer
      - .actual_access:  read_only
        .address_space:  global
        .offset:         56
        .size:           8
        .value_kind:     global_buffer
      - .offset:         64
        .size:           4
        .value_kind:     by_value
      - .actual_access:  write_only
        .address_space:  global
        .offset:         72
        .size:           8
        .value_kind:     global_buffer
      - .offset:         80
        .size:           4
        .value_kind:     by_value
    .group_segment_fixed_size: 128
    .kernarg_segment_align: 8
    .kernarg_segment_size: 84
    .language:       OpenCL C
    .language_version:
      - 2
      - 0
    .max_flat_workgroup_size: 256
    .name:           _Z12graph_kerneliPKfS0_S0_PKtiS2_S2_iPti
    .private_segment_fixed_size: 0
    .sgpr_count:     48
    .sgpr_spill_count: 0
    .symbol:         _Z12graph_kerneliPKfS0_S0_PKtiS2_S2_iPti.kd
    .uniform_work_group_size: 1
    .uses_dynamic_stack: false
    .vgpr_count:     75
    .vgpr_spill_count: 0
    .wavefront_size: 64
  - .agpr_count:     0
    .args:
      - .offset:         0
        .size:           96
        .value_kind:     by_value
      - .offset:         96
        .size:           336
        .value_kind:     by_value
      - .offset:         432
        .size:           328
        .value_kind:     by_value
    .group_segment_fixed_size: 50688
    .kernarg_segment_align: 8
    .kernarg_segment_size: 760
    .language:       OpenCL C
    .language_version:
      - 2
      - 0
    .max_flat_workgroup_size: 512
    .name:           _Z12front_kernel9FrontArgs8PrepArgs8FragArgs
    .private_segment_fixed_size: 0
    .sgpr_count:     58
    .sgpr_spill_count: 0
    .symbol:         _Z12front_kernel9FrontArgs8PrepArgs8FragArgs.kd
    .uniform_work_group_size: 1
    .uses_dynamic_stack: false
    .vgpr_count:     61
    .vgpr_spill_count: 0
    .wavefront_size: 64
  - .agpr_count:     0
    .args:
      - .offset:         0
        .size:           144
        .value_kind:     by_value
    .group_segment_fixed_size: 131072
    .kernarg_segment_align: 8
    .kernarg_segment_size: 144
    .language:       OpenCL C
    .language_version:
      - 2
      - 0
    .max_flat_workgroup_size: 512
    .name:           _Z13gemm8p_kernel5GArgs
    .private_segment_fixed_size: 0
    .sgpr_count:     42
    .sgpr_spill_count: 0
    .symbol:         _Z13gemm8p_kernel5GArgs.kd
    .uniform_work_group_size: 1
    .uses_dynamic_stack: false
    .vgpr_count:     250
    .vgpr_spill_count: 0
    .wavefront_size: 64
  - .agpr_count:     0
    .args:
      - .actual_access:  read_only
        .address_space:  global
        .offset:         0
        .size:           8
        .value_kind:     global_buffer
      - .offset:         8
        .size:           4
        .value_kind:     by_value
      - .address_space:  global
        .offset:         16
        .size:           8
        .value_kind:     global_buffer
      - .offset:         24
        .size:           4
        .value_kind:     by_value
      - .address_space:  global
        .offset:         32
        .size:           8
        .value_kind:     global_buffer
      - .offset:         40
        .size:           4
        .value_kind:     by_value
      - .actual_access:  write_only
        .address_space:  global
        .offset:         48
        .size:           8
        .value_kind:     global_buffer
      - .offset:         56
        .size:           4
        .value_kind:     by_value
      - .offset:         64
        .size:           112
        .value_kind:     by_value
    .group_segment_fixed_size: 83968
    .kernarg_segment_align: 8
    .kernarg_segment_size: 176
    .language:       OpenCL C
    .language_version:
      - 2
      - 0
    .max_flat_workgroup_size: 512
    .name:           _Z11attn_kernelPKtiS0_iS0_iPti6CoArgs
    .private_segment_fixed_size: 0
    .sgpr_count:     74
    .sgpr_spill_count: 0
    .symbol:         _Z11attn_kernelPKtiS0_iS0_iPti6CoArgs.kd
    .uniform_work_group_size: 1
    .uses_dynamic_stack: false
    .vgpr_count:     218
    .vgpr_spill_count: 0
    .wavefront_size: 64
  - .agpr_count:     0
    .args:
      - .offset:         0
        .size:           144
        .value_kind:     by_value
    .group_segment_fixed_size: 77312
    .kernarg_segment_align: 8
    .kernarg_segment_size: 144
    .language:       OpenCL C
    .language_version:
      - 2
      - 0
    .max_flat_workgroup_size: 512
    .name:           _Z12chain_kernelILi0EEv9ChainArgs
    .private_segment_fixed_size: 0
    .sgpr_count:     35
    .sgpr_spill_count: 0
    .symbol:         _Z12chain_kernelILi0EEv9ChainArgs.kd
    .uniform_work_group_size: 1
    .uses_dynamic_stack: false
    .vgpr_count:     224
    .vgpr_spill_count: 0
    .wavefront_size: 64
  - .agpr_count:     0
    .args:
      - .offset:         0
        .size:           144
        .value_kind:     by_value
    .group_segment_fixed_size: 77312
    .kernarg_segment_align: 8
    .kernarg_segment_size: 144
    .language:       OpenCL C
    .language_version:
      - 2
      - 0
    .max_flat_workgroup_size: 512
    .name:           _Z12chain_kernelILi1EEv9ChainArgs
    .private_segment_fixed_size: 0
    .sgpr_count:     35
    .sgpr_spill_count: 0
    .symbol:         _Z12chain_kernelILi1EEv9ChainArgs.kd
    .uniform_work_group_size: 1
    .uses_dynamic_stack: false
    .vgpr_count:     210
    .vgpr_spill_count: 0
    .wavefront_size: 64
